# P1b: add wave-group stagger (waves 4-7 carry second-half MFMAs across the stage barrier) on top of the straight-line swap bodies
# speedup vs baseline: 1.0357x; 1.0024x over previous
.LBB0_231:
	s_waitcnt lgkmcnt(0)
	s_barrier
	s_cmp_lt_u32 s15, 0x4000
	s_cbranch_scc1 .Lp1b_nodef
	s_cmp_eq_u32 s1, 0
	s_cbranch_scc1 .Lp1b_nodef
	s_cmp_eq_u32 s16, 0
	s_cbranch_scc1 .Lp1b_nodef
	s_cmp_lg_u32 s26, 0
	s_cbranch_scc1 .Lp1b_defT
	v_mfma_scale_f32_16x16x128_f8f6f4 v[130:133], v[58:65], v[26:33], v[130:133], v218, v218 op_sel_hi:[0,0,0]
	v_mfma_scale_f32_16x16x128_f8f6f4 v[126:129], v[58:65], v[18:25], v[126:129], v218, v218 op_sel_hi:[0,0,0]
	v_mfma_scale_f32_16x16x128_f8f6f4 v[122:125], v[58:65], v[10:17], v[122:125], v218, v218 op_sel_hi:[0,0,0]
	v_mfma_scale_f32_16x16x128_f8f6f4 v[118:121], v[58:65], v[2:9], v[118:121], v218, v218 op_sel_hi:[0,0,0]
	v_mfma_scale_f32_16x16x128_f8f6f4 v[114:117], v[42:49], v[26:33], v[114:117], v218, v218 op_sel_hi:[0,0,0]
	v_mfma_scale_f32_16x16x128_f8f6f4 v[110:113], v[42:49], v[18:25], v[110:113], v218, v218 op_sel_hi:[0,0,0]
	v_mfma_scale_f32_16x16x128_f8f6f4 v[106:109], v[42:49], v[10:17], v[106:109], v218, v218 op_sel_hi:[0,0,0]
	v_mfma_scale_f32_16x16x128_f8f6f4 v[102:105], v[42:49], v[2:9], v[102:105], v218, v218 op_sel_hi:[0,0,0]
	v_mfma_scale_f32_16x16x128_f8f6f4 v[98:101], v[50:57], v[26:33], v[98:101], v218, v218 op_sel_hi:[0,0,0]
	v_mfma_scale_f32_16x16x128_f8f6f4 v[94:97], v[50:57], v[18:25], v[94:97], v218, v218 op_sel_hi:[0,0,0]
	v_mfma_scale_f32_16x16x128_f8f6f4 v[90:93], v[50:57], v[10:17], v[90:93], v218, v218 op_sel_hi:[0,0,0]
	v_mfma_scale_f32_16x16x128_f8f6f4 v[86:89], v[50:57], v[2:9], v[86:89], v218, v218 op_sel_hi:[0,0,0]
	v_mfma_scale_f32_16x16x128_f8f6f4 v[82:85], v[34:41], v[26:33], v[82:85], v218, v218 op_sel_hi:[0,0,0]
	v_mfma_scale_f32_16x16x128_f8f6f4 v[78:81], v[34:41], v[18:25], v[78:81], v218, v218 op_sel_hi:[0,0,0]
	v_mfma_scale_f32_16x16x128_f8f6f4 v[74:77], v[34:41], v[10:17], v[74:77], v218, v218 op_sel_hi:[0,0,0]
	v_mfma_scale_f32_16x16x128_f8f6f4 v[70:73], v[34:41], v[2:9], v[70:73], v218, v218 op_sel_hi:[0,0,0]
	s_branch .Lp1b_nodef
.Lp1b_defT:
	v_mfma_scale_f32_16x16x128_f8f6f4 v[130:133], v[26:33], v[58:65], v[130:133], v218, v218 op_sel_hi:[0,0,0]
	v_mfma_scale_f32_16x16x128_f8f6f4 v[126:129], v[18:25], v[58:65], v[126:129], v218, v218 op_sel_hi:[0,0,0]
	v_mfma_scale_f32_16x16x128_f8f6f4 v[122:125], v[10:17], v[58:65], v[122:125], v218, v218 op_sel_hi:[0,0,0]
	v_mfma_scale_f32_16x16x128_f8f6f4 v[118:121], v[2:9], v[58:65], v[118:121], v218, v218 op_sel_hi:[0,0,0]
	v_mfma_scale_f32_16x16x128_f8f6f4 v[114:117], v[26:33], v[42:49], v[114:117], v218, v218 op_sel_hi:[0,0,0]
	v_mfma_scale_f32_16x16x128_f8f6f4 v[110:113], v[18:25], v[42:49], v[110:113], v218, v218 op_sel_hi:[0,0,0]
	v_mfma_scale_f32_16x16x128_f8f6f4 v[106:109], v[10:17], v[42:49], v[106:109], v218, v218 op_sel_hi:[0,0,0]
	v_mfma_scale_f32_16x16x128_f8f6f4 v[102:105], v[2:9], v[42:49], v[102:105], v218, v218 op_sel_hi:[0,0,0]
	v_mfma_scale_f32_16x16x128_f8f6f4 v[98:101], v[26:33], v[50:57], v[98:101], v218, v218 op_sel_hi:[0,0,0]
	v_mfma_scale_f32_16x16x128_f8f6f4 v[94:97], v[18:25], v[50:57], v[94:97], v218, v218 op_sel_hi:[0,0,0]
	v_mfma_scale_f32_16x16x128_f8f6f4 v[90:93], v[10:17], v[50:57], v[90:93], v218, v218 op_sel_hi:[0,0,0]
	v_mfma_scale_f32_16x16x128_f8f6f4 v[86:89], v[2:9], v[50:57], v[86:89], v218, v218 op_sel_hi:[0,0,0]
	v_mfma_scale_f32_16x16x128_f8f6f4 v[82:85], v[26:33], v[34:41], v[82:85], v218, v218 op_sel_hi:[0,0,0]
	v_mfma_scale_f32_16x16x128_f8f6f4 v[78:81], v[18:25], v[34:41], v[78:81], v218, v218 op_sel_hi:[0,0,0]
	v_mfma_scale_f32_16x16x128_f8f6f4 v[74:77], v[10:17], v[34:41], v[74:77], v218, v218 op_sel_hi:[0,0,0]
	v_mfma_scale_f32_16x16x128_f8f6f4 v[70:73], v[2:9], v[34:41], v[70:73], v218, v218 op_sel_hi:[0,0,0]
.Lp1b_nodef:
	s_andn2_b64 vcc, exec, s[22:23]
	s_cbranch_vccnz .LBB0_244
	s_lshl_b32 s5, s21, 16
	s_lshl_b32 s22, s9, 6
	s_and_b32 s5, s5, 0x10000
	s_ashr_i32 s23, s22, 31
	s_lshl_b64 s[22:23], s[22:23], 1
	s_add_i32 s5, s15, s5
	v_lshl_add_u64 v[2:3], v[198:199], 0, s[22:23]
	s_mov_b32 m0, s5
	s_add_i32 s9, s9, 1
	global_load_lds_dwordx4 v[2:3], off
	v_lshl_add_u64 v[2:3], v[200:201], 0, s[22:23]
	s_add_i32 m0, s5, 0x400
	s_nop 0
	global_load_lds_dwordx4 v[2:3], off
	v_lshl_add_u64 v[2:3], v[202:203], 0, s[22:23]
	s_add_i32 m0, s5, 0x800
	s_nop 0
	global_load_lds_dwordx4 v[2:3], off
	v_lshl_add_u64 v[2:3], v[204:205], 0, s[22:23]
	s_add_i32 m0, s5, 0xc00
	s_nop 0
	global_load_lds_dwordx4 v[2:3], off
	v_lshl_add_u64 v[2:3], v[206:207], 0, s[22:23]
	s_add_i32 m0, s5, 0x8000
	s_nop 0
	global_load_lds_dwordx4 v[2:3], off
	v_lshl_add_u64 v[2:3], v[208:209], 0, s[22:23]
	s_add_i32 m0, s5, 0x8400
	s_nop 0
	global_load_lds_dwordx4 v[2:3], off
	v_lshl_add_u64 v[2:3], v[210:211], 0, s[22:23]
	s_add_i32 m0, s5, 0x8800
	s_nop 0
	global_load_lds_dwordx4 v[2:3], off
	v_lshl_add_u64 v[2:3], v[212:213], 0, s[22:23]
	s_add_i32 m0, s5, 0x8c00
	s_cmp_lg_u32 s9, 8
	global_load_lds_dwordx4 v[2:3], off
	s_mov_b64 s[22:23], -1
	s_cbranch_scc1 .LBB0_247
	s_andn2_b64 vcc, exec, s[12:13]
	s_cbranch_vccnz .LBB0_245
	s_add_i32 s5, s62, 2
	s_mul_i32 s9, s5, s3
	s_add_i32 s9, s9, s69
	v_mov_b32_e32 v3, v0
	v_mov_b32_e32 v2, v0
	s_cmpk_gt_i32 s9, 0x8f
	s_cbranch_scc0 .LBB0_237
	s_cmpk_gt_u32 s9, 0x94
	s_cselect_b64 s[12:13], -1, 0
	s_or_b64 s[12:13], s[18:19], s[12:13]
	s_mov_b64 s[22:23], 0
	s_and_b64 vcc, exec, s[12:13]
	s_mov_b64 s[12:13], 0
	s_mov_b32 s30, s10
	s_mov_b32 s5, s8
	s_cbranch_vccnz .LBB0_237
	s_add_i32 s5, s9, 0xffffff74
	s_cmpk_lg_i32 s9, 0x90
	s_cselect_b32 s5, s5, 2
	s_mov_b64 s[12:13], -1
	s_mov_b32 s30, s56

.LBB0_248:
	s_cmp_lt_u32 s15, 0x4000
	s_cbranch_scc0 .Lp1b_Y
	s_cmp_lg_u32 s26, 0
	s_cbranch_scc1 .Lp1b_XT
	s_and_b32 s5, s4, 0x10000
	v_or_b32_e32 v2, s5, v250
	v_xor_b32_e32 v6, 64, v2
	v_add_u32_e32 v68, s5, v249
	v_xor_b32_e32 v66, 64, v68
	ds_read_b128 v[26:29], v2 offset:0
	ds_read_b128 v[30:33], v6 offset:0
	ds_read_b128 v[18:21], v2 offset:2048
	ds_read_b128 v[22:25], v6 offset:2048
	ds_read_b128 v[10:13], v2 offset:4096
	ds_read_b128 v[14:17], v6 offset:4096
	ds_read_b128 v[2:5], v2 offset:6144
	ds_read_b128 v[6:9], v6 offset:6144
	ds_read_b128 v[58:61], v68 offset:0
	ds_read_b128 v[62:65], v66 offset:0
	ds_read_b128 v[42:45], v68 offset:2048
	ds_read_b128 v[46:49], v66 offset:2048
	ds_read_b128 v[50:53], v68 offset:4096
	ds_read_b128 v[54:57], v66 offset:4096
	ds_read_b128 v[34:37], v68 offset:6144
	ds_read_b128 v[38:41], v66 offset:6144
	s_waitcnt lgkmcnt(4)
	s_nop 0
	v_mfma_scale_f32_16x16x128_f8f6f4 v[194:197], v[58:65], v[26:33], v[194:197], v218, v218 op_sel_hi:[0,0,0]
	v_mfma_scale_f32_16x16x128_f8f6f4 v[190:193], v[58:65], v[18:25], v[190:193], v218, v218 op_sel_hi:[0,0,0]
	v_mfma_scale_f32_16x16x128_f8f6f4 v[186:189], v[58:65], v[10:17], v[186:189], v218, v218 op_sel_hi:[0,0,0]
	v_mfma_scale_f32_16x16x128_f8f6f4 v[182:185], v[58:65], v[2:9], v[182:185], v218, v218 op_sel_hi:[0,0,0]
	v_mfma_scale_f32_16x16x128_f8f6f4 v[178:181], v[42:49], v[26:33], v[178:181], v218, v218 op_sel_hi:[0,0,0]
	v_mfma_scale_f32_16x16x128_f8f6f4 v[174:177], v[42:49], v[18:25], v[174:177], v218, v218 op_sel_hi:[0,0,0]
	v_mfma_scale_f32_16x16x128_f8f6f4 v[170:173], v[42:49], v[10:17], v[170:173], v218, v218 op_sel_hi:[0,0,0]
	v_mfma_scale_f32_16x16x128_f8f6f4 v[166:169], v[42:49], v[2:9], v[166:169], v218, v218 op_sel_hi:[0,0,0]
	ds_read_b128 v[58:61], v68 offset:8192
	ds_read_b128 v[62:65], v66 offset:8192
	ds_read_b128 v[42:45], v68 offset:10240
	ds_read_b128 v[46:49], v66 offset:10240
	s_waitcnt lgkmcnt(4)
	v_mfma_scale_f32_16x16x128_f8f6f4 v[162:165], v[50:57], v[26:33], v[162:165], v218, v218 op_sel_hi:[0,0,0]
	v_mfma_scale_f32_16x16x128_f8f6f4 v[158:161], v[50:57], v[18:25], v[158:161], v218, v218 op_sel_hi:[0,0,0]
	v_mfma_scale_f32_16x16x128_f8f6f4 v[154:157], v[50:57], v[10:17], v[154:157], v218, v218 op_sel_hi:[0,0,0]
	v_mfma_scale_f32_16x16x128_f8f6f4 v[150:153], v[50:57], v[2:9], v[150:153], v218, v218 op_sel_hi:[0,0,0]
	v_mfma_scale_f32_16x16x128_f8f6f4 v[146:149], v[34:41], v[26:33], v[146:149], v218, v218 op_sel_hi:[0,0,0]
	v_mfma_scale_f32_16x16x128_f8f6f4 v[142:145], v[34:41], v[18:25], v[142:145], v218, v218 op_sel_hi:[0,0,0]
	v_mfma_scale_f32_16x16x128_f8f6f4 v[138:141], v[34:41], v[10:17], v[138:141], v218, v218 op_sel_hi:[0,0,0]
	v_mfma_scale_f32_16x16x128_f8f6f4 v[134:137], v[34:41], v[2:9], v[134:137], v218, v218 op_sel_hi:[0,0,0]
	ds_read_b128 v[50:53], v68 offset:12288
	ds_read_b128 v[54:57], v66 offset:12288
	ds_read_b128 v[34:37], v68 offset:14336
	ds_read_b128 v[38:41], v66 offset:14336
	s_waitcnt lgkmcnt(4)
	v_mfma_scale_f32_16x16x128_f8f6f4 v[130:133], v[58:65], v[26:33], v[130:133], v218, v218 op_sel_hi:[0,0,0]
	v_mfma_scale_f32_16x16x128_f8f6f4 v[126:129], v[58:65], v[18:25], v[126:129], v218, v218 op_sel_hi:[0,0,0]
	v_mfma_scale_f32_16x16x128_f8f6f4 v[122:125], v[58:65], v[10:17], v[122:125], v218, v218 op_sel_hi:[0,0,0]
	v_mfma_scale_f32_16x16x128_f8f6f4 v[118:121], v[58:65], v[2:9], v[118:121], v218, v218 op_sel_hi:[0,0,0]
	v_mfma_scale_f32_16x16x128_f8f6f4 v[114:117], v[42:49], v[26:33], v[114:117], v218, v218 op_sel_hi:[0,0,0]
	v_mfma_scale_f32_16x16x128_f8f6f4 v[110:113], v[42:49], v[18:25], v[110:113], v218, v218 op_sel_hi:[0,0,0]
	v_mfma_scale_f32_16x16x128_f8f6f4 v[106:109], v[42:49], v[10:17], v[106:109], v218, v218 op_sel_hi:[0,0,0]
	v_mfma_scale_f32_16x16x128_f8f6f4 v[102:105], v[42:49], v[2:9], v[102:105], v218, v218 op_sel_hi:[0,0,0]
	s_waitcnt lgkmcnt(0)
	v_mfma_scale_f32_16x16x128_f8f6f4 v[98:101], v[50:57], v[26:33], v[98:101], v218, v218 op_sel_hi:[0,0,0]
	v_mfma_scale_f32_16x16x128_f8f6f4 v[94:97], v[50:57], v[18:25], v[94:97], v218, v218 op_sel_hi:[0,0,0]
	v_mfma_scale_f32_16x16x128_f8f6f4 v[90:93], v[50:57], v[10:17], v[90:93], v218, v218 op_sel_hi:[0,0,0]
	v_mfma_scale_f32_16x16x128_f8f6f4 v[86:89], v[50:57], v[2:9], v[86:89], v218, v218 op_sel_hi:[0,0,0]
	v_mfma_scale_f32_16x16x128_f8f6f4 v[82:85], v[34:41], v[26:33], v[82:85], v218, v218 op_sel_hi:[0,0,0]
	v_mfma_scale_f32_16x16x128_f8f6f4 v[78:81], v[34:41], v[18:25], v[78:81], v218, v218 op_sel_hi:[0,0,0]
	v_mfma_scale_f32_16x16x128_f8f6f4 v[74:77], v[34:41], v[10:17], v[74:77], v218, v218 op_sel_hi:[0,0,0]
	v_mfma_scale_f32_16x16x128_f8f6f4 v[70:73], v[34:41], v[2:9], v[70:73], v218, v218 op_sel_hi:[0,0,0]
	s_branch .LBB0_225

.Lp1b_Y:
	s_cmp_lg_u32 s26, 0
	s_cbranch_scc1 .Lp1b_YT
	s_and_b32 s5, s4, 0x10000
	v_or_b32_e32 v2, s5, v250
	v_xor_b32_e32 v6, 64, v2
	v_add_u32_e32 v68, s5, v249
	v_xor_b32_e32 v66, 64, v68
	ds_read_b128 v[26:29], v2 offset:0
	ds_read_b128 v[30:33], v6 offset:0
	ds_read_b128 v[18:21], v2 offset:2048
	ds_read_b128 v[22:25], v6 offset:2048
	ds_read_b128 v[10:13], v2 offset:4096
	ds_read_b128 v[14:17], v6 offset:4096
	ds_read_b128 v[2:5], v2 offset:6144
	ds_read_b128 v[6:9], v6 offset:6144
	ds_read_b128 v[58:61], v68 offset:0
	ds_read_b128 v[62:65], v66 offset:0
	ds_read_b128 v[42:45], v68 offset:2048
	ds_read_b128 v[46:49], v66 offset:2048
	ds_read_b128 v[50:53], v68 offset:4096
	ds_read_b128 v[54:57], v66 offset:4096
	ds_read_b128 v[34:37], v68 offset:6144
	ds_read_b128 v[38:41], v66 offset:6144
	s_waitcnt lgkmcnt(4)
	s_nop 0
	v_mfma_scale_f32_16x16x128_f8f6f4 v[194:197], v[58:65], v[26:33], v[194:197], v218, v218 op_sel_hi:[0,0,0]
	v_mfma_scale_f32_16x16x128_f8f6f4 v[190:193], v[58:65], v[18:25], v[190:193], v218, v218 op_sel_hi:[0,0,0]
	v_mfma_scale_f32_16x16x128_f8f6f4 v[186:189], v[58:65], v[10:17], v[186:189], v218, v218 op_sel_hi:[0,0,0]
	v_mfma_scale_f32_16x16x128_f8f6f4 v[182:185], v[58:65], v[2:9], v[182:185], v218, v218 op_sel_hi:[0,0,0]
	v_mfma_scale_f32_16x16x128_f8f6f4 v[178:181], v[42:49], v[26:33], v[178:181], v218, v218 op_sel_hi:[0,0,0]
	v_mfma_scale_f32_16x16x128_f8f6f4 v[174:177], v[42:49], v[18:25], v[174:177], v218, v218 op_sel_hi:[0,0,0]
	v_mfma_scale_f32_16x16x128_f8f6f4 v[170:173], v[42:49], v[10:17], v[170:173], v218, v218 op_sel_hi:[0,0,0]
	v_mfma_scale_f32_16x16x128_f8f6f4 v[166:169], v[42:49], v[2:9], v[166:169], v218, v218 op_sel_hi:[0,0,0]
	ds_read_b128 v[58:61], v68 offset:8192
	ds_read_b128 v[62:65], v66 offset:8192
	ds_read_b128 v[42:45], v68 offset:10240
	ds_read_b128 v[46:49], v66 offset:10240
	s_waitcnt lgkmcnt(4)
	v_mfma_scale_f32_16x16x128_f8f6f4 v[162:165], v[50:57], v[26:33], v[162:165], v218, v218 op_sel_hi:[0,0,0]
	v_mfma_scale_f32_16x16x128_f8f6f4 v[158:161], v[50:57], v[18:25], v[158:161], v218, v218 op_sel_hi:[0,0,0]
	v_mfma_scale_f32_16x16x128_f8f6f4 v[154:157], v[50:57], v[10:17], v[154:157], v218, v218 op_sel_hi:[0,0,0]
	v_mfma_scale_f32_16x16x128_f8f6f4 v[150:153], v[50:57], v[2:9], v[150:153], v218, v218 op_sel_hi:[0,0,0]
	v_mfma_scale_f32_16x16x128_f8f6f4 v[146:149], v[34:41], v[26:33], v[146:149], v218, v218 op_sel_hi:[0,0,0]
	v_mfma_scale_f32_16x16x128_f8f6f4 v[142:145], v[34:41], v[18:25], v[142:145], v218, v218 op_sel_hi:[0,0,0]
	v_mfma_scale_f32_16x16x128_f8f6f4 v[138:141], v[34:41], v[10:17], v[138:141], v218, v218 op_sel_hi:[0,0,0]
	v_mfma_scale_f32_16x16x128_f8f6f4 v[134:137], v[34:41], v[2:9], v[134:137], v218, v218 op_sel_hi:[0,0,0]
	ds_read_b128 v[50:53], v68 offset:12288
	ds_read_b128 v[54:57], v66 offset:12288
	ds_read_b128 v[34:37], v68 offset:14336
	ds_read_b128 v[38:41], v66 offset:14336
	s_waitcnt lgkmcnt(0)
	s_branch .LBB0_225
; #define GS_WAIT(ahead) do { if ((ahead) >= 1) asm volatile("s_waitcnt vmcnt(8)" ::: "memory"); else asm volatile("s_waitcnt vmcnt(0)" ::: "memory"); } while (0)
; #define GS_WAIT(ahead) do { if ((ahead) >= 2) asm volatile("s_waitcnt vmcnt(8)" ::: "memory"); else if ((ahead) == 1) asm volatile("s_waitcnt vmcnt(4)" ::: "memory"); \
;         else asm volatile("s_waitcnt vmcnt(0)" ::: "memory"); } while (0)
; template <class PH>
; __device__ __forceinline__ void gemm_stream(unsigned char* smem, PH& ph) {
;     ...
;         if (computed < issued) { GS_WAIT(0); prewaited = true; }
;         asm volatile("s_waitcnt lgkmcnt(0)" ::: "memory"); __builtin_amdgcn_s_barrier(); asm volatile("" ::: "memory");
;         ph.epilogue(acc, d_cmp, smem + ((computed + 1) & 1) * 65536 + wid * STG_WAVE);
.Lp1b_YT:
	s_and_b32 s5, s4, 0x10000
	v_or_b32_e32 v2, s5, v250
	v_xor_b32_e32 v6, 64, v2
	v_add_u32_e32 v68, s5, v249
	v_xor_b32_e32 v66, 64, v68
	ds_read_b128 v[26:29], v2 offset:0
	ds_read_b128 v[30:33], v6 offset:0
	ds_read_b128 v[18:21], v2 offset:2048
	ds_read_b128 v[22:25], v6 offset:2048
	ds_read_b128 v[10:13], v2 offset:4096
	ds_read_b128 v[14:17], v6 offset:4096
	ds_read_b128 v[2:5], v2 offset:6144
	ds_read_b128 v[6:9], v6 offset:6144
	ds_read_b128 v[58:61], v68 offset:0
	ds_read_b128 v[62:65], v66 offset:0
	ds_read_b128 v[42:45], v68 offset:2048
	ds_read_b128 v[46:49], v66 offset:2048
	ds_read_b128 v[50:53], v68 offset:4096
	ds_read_b128 v[54:57], v66 offset:4096
	ds_read_b128 v[34:37], v68 offset:6144
	ds_read_b128 v[38:41], v66 offset:6144
	s_waitcnt lgkmcnt(4)
	s_nop 0
	v_mfma_scale_f32_16x16x128_f8f6f4 v[194:197], v[26:33], v[58:65], v[194:197], v218, v218 op_sel_hi:[0,0,0]
	v_mfma_scale_f32_16x16x128_f8f6f4 v[190:193], v[18:25], v[58:65], v[190:193], v218, v218 op_sel_hi:[0,0,0]
	v_mfma_scale_f32_16x16x128_f8f6f4 v[186:189], v[10:17], v[58:65], v[186:189], v218, v218 op_sel_hi:[0,0,0]
	v_mfma_scale_f32_16x16x128_f8f6f4 v[182:185], v[2:9], v[58:65], v[182:185], v218, v218 op_sel_hi:[0,0,0]
	v_mfma_scale_f32_16x16x128_f8f6f4 v[178:181], v[26:33], v[42:49], v[178:181], v218, v218 op_sel_hi:[0,0,0]
	v_mfma_scale_f32_16x16x128_f8f6f4 v[174:177], v[18:25], v[42:49], v[174:177], v218, v218 op_sel_hi:[0,0,0]
	v_mfma_scale_f32_16x16x128_f8f6f4 v[170:173], v[10:17], v[42:49], v[170:173], v218, v218 op_sel_hi:[0,0,0]
	v_mfma_scale_f32_16x16x128_f8f6f4 v[166:169], v[2:9], v[42:49], v[166:169], v218, v218 op_sel_hi:[0,0,0]
	ds_read_b128 v[58:61], v68 offset:8192
	ds_read_b128 v[62:65], v66 offset:8192
	ds_read_b128 v[42:45], v68 offset:10240
	ds_read_b128 v[46:49], v66 offset:10240
	s_waitcnt lgkmcnt(4)
	v_mfma_scale_f32_16x16x128_f8f6f4 v[162:165], v[26:33], v[50:57], v[162:165], v218, v218 op_sel_hi:[0,0,0]
	v_mfma_scale_f32_16x16x128_f8f6f4 v[158:161], v[18:25], v[50:57], v[158:161], v218, v218 op_sel_hi:[0,0,0]
	v_mfma_scale_f32_16x16x128_f8f6f4 v[154:157], v[10:17], v[50:57], v[154:157], v218, v218 op_sel_hi:[0,0,0]
	v_mfma_scale_f32_16x16x128_f8f6f4 v[150:153], v[2:9], v[50:57], v[150:153], v218, v218 op_sel_hi:[0,0,0]
	v_mfma_scale_f32_16x16x128_f8f6f4 v[146:149], v[26:33], v[34:41], v[146:149], v218, v218 op_sel_hi:[0,0,0]
	v_mfma_scale_f32_16x16x128_f8f6f4 v[142:145], v[18:25], v[34:41], v[142:145], v218, v218 op_sel_hi:[0,0,0]
	v_mfma_scale_f32_16x16x128_f8f6f4 v[138:141], v[10:17], v[34:41], v[138:141], v218, v218 op_sel_hi:[0,0,0]
	v_mfma_scale_f32_16x16x128_f8f6f4 v[134:137], v[2:9], v[34:41], v[134:137], v218, v218 op_sel_hi:[0,0,0]
	ds_read_b128 v[50:53], v68 offset:12288
	ds_read_b128 v[54:57], v66 offset:12288
	ds_read_b128 v[34:37], v68 offset:14336
	ds_read_b128 v[38:41], v66 offset:14336
	s_waitcnt lgkmcnt(0)
	s_branch .LBB0_225
.LBB0_280:
	s_cmp_lt_u32 s15, 0x4000
	s_cbranch_scc1 .Lp1b_notail
	s_cmp_eq_u32 s16, 0
	s_cbranch_scc1 .Lp1b_notail
	s_cmp_lg_u32 s26, 0
	s_cbranch_scc1 .Lp1b_tailT
	v_mfma_scale_f32_16x16x128_f8f6f4 v[130:133], v[58:65], v[26:33], v[130:133], v218, v218 op_sel_hi:[0,0,0]
	v_mfma_scale_f32_16x16x128_f8f6f4 v[126:129], v[58:65], v[18:25], v[126:129], v218, v218 op_sel_hi:[0,0,0]
	v_mfma_scale_f32_16x16x128_f8f6f4 v[122:125], v[58:65], v[10:17], v[122:125], v218, v218 op_sel_hi:[0,0,0]
	v_mfma_scale_f32_16x16x128_f8f6f4 v[118:121], v[58:65], v[2:9], v[118:121], v218, v218 op_sel_hi:[0,0,0]
	v_mfma_scale_f32_16x16x128_f8f6f4 v[114:117], v[42:49], v[26:33], v[114:117], v218, v218 op_sel_hi:[0,0,0]
	v_mfma_scale_f32_16x16x128_f8f6f4 v[110:113], v[42:49], v[18:25], v[110:113], v218, v218 op_sel_hi:[0,0,0]
	v_mfma_scale_f32_16x16x128_f8f6f4 v[106:109], v[42:49], v[10:17], v[106:109], v218, v218 op_sel_hi:[0,0,0]
	v_mfma_scale_f32_16x16x128_f8f6f4 v[102:105], v[42:49], v[2:9], v[102:105], v218, v218 op_sel_hi:[0,0,0]
	v_mfma_scale_f32_16x16x128_f8f6f4 v[98:101], v[50:57], v[26:33], v[98:101], v218, v218 op_sel_hi:[0,0,0]
	v_mfma_scale_f32_16x16x128_f8f6f4 v[94:97], v[50:57], v[18:25], v[94:97], v218, v218 op_sel_hi:[0,0,0]
	v_mfma_scale_f32_16x16x128_f8f6f4 v[90:93], v[50:57], v[10:17], v[90:93], v218, v218 op_sel_hi:[0,0,0]
	v_mfma_scale_f32_16x16x128_f8f6f4 v[86:89], v[50:57], v[2:9], v[86:89], v218, v218 op_sel_hi:[0,0,0]
	v_mfma_scale_f32_16x16x128_f8f6f4 v[82:85], v[34:41], v[26:33], v[82:85], v218, v218 op_sel_hi:[0,0,0]
	v_mfma_scale_f32_16x16x128_f8f6f4 v[78:81], v[34:41], v[18:25], v[78:81], v218, v218 op_sel_hi:[0,0,0]
	v_mfma_scale_f32_16x16x128_f8f6f4 v[74:77], v[34:41], v[10:17], v[74:77], v218, v218 op_sel_hi:[0,0,0]
	v_mfma_scale_f32_16x16x128_f8f6f4 v[70:73], v[34:41], v[2:9], v[70:73], v218, v218 op_sel_hi:[0,0,0]
	s_branch .Lp1b_notail
